# speedup vs baseline: 1.0121x; 1.0016x over previous
.LBB1_52:
	ds_read_b128 v[138:141], v135
	ds_read_b128 v[142:145], v135 offset:1024
	ds_read_b128 v[146:149], v135 offset:2048
	ds_read_b128 v[150:153], v135 offset:3072
	ds_read_b128 v[154:157], v135 offset:4096
	ds_read_b128 v[158:161], v135 offset:5120
	s_add_u32 m0, s12, 0xc000
	ds_read_b128 v[162:165], v121
	ds_read_b128 v[182:185], v121 offset:1024
	ds_read_b128 v[186:189], v108
	ds_read_b128 v[190:193], v108 offset:1024
	global_load_lds_dwordx4 v236, s[8:9]
	s_add_u32 m0, s12, 0xe000
	s_nop 0
	global_load_lds_dwordx4 v237, s[8:9]
	s_waitcnt lgkmcnt(4)
	s_barrier
	s_waitcnt lgkmcnt(0)
	v_mfma_f32_16x16x32_f16 v[94:97], v[162:165], v[138:141], v[94:97]
	v_mfma_f32_16x16x32_f16 v[90:93], v[162:165], v[146:149], v[90:93]
	v_mfma_f32_16x16x32_f16 v[86:89], v[162:165], v[154:157], v[86:89]
	v_mfma_f32_16x16x32_f16 v[82:85], v[186:189], v[138:141], v[82:85]
	v_mfma_f32_16x16x32_f16 v[78:81], v[186:189], v[146:149], v[78:81]
	v_mfma_f32_16x16x32_f16 v[66:69], v[186:189], v[154:157], v[66:69]
	v_mfma_f32_16x16x32_f16 v[94:97], v[182:185], v[142:145], v[94:97]
	v_mfma_f32_16x16x32_f16 v[90:93], v[182:185], v[150:153], v[90:93]
	v_mfma_f32_16x16x32_f16 v[86:89], v[182:185], v[158:161], v[86:89]
	v_mfma_f32_16x16x32_f16 v[82:85], v[190:193], v[142:145], v[82:85]
	v_mfma_f32_16x16x32_f16 v[78:81], v[190:193], v[150:153], v[78:81]
	v_mfma_f32_16x16x32_f16 v[66:69], v[190:193], v[158:161], v[66:69]
	s_barrier
	s_add_u32 m0, s12, 0x10000
	ds_read_b128 v[194:197], v134
	ds_read_b128 v[198:201], v134 offset:1024
	ds_read_b128 v[202:205], v134 offset:2048
	ds_read_b128 v[206:209], v134 offset:3072
	ds_read_b128 v[210:213], v134 offset:4096
	ds_read_b128 v[214:217], v134 offset:5120
	global_load_lds_dwordx4 v240, s[10:11]
	s_add_u32 m0, s12, 0x12000
	s_nop 0
	global_load_lds_dwordx4 v241, s[10:11]
	s_barrier
	s_waitcnt lgkmcnt(0)
	v_mfma_f32_16x16x32_f16 v[22:25], v[162:165], v[194:197], v[22:25]
	v_mfma_f32_16x16x32_f16 v[18:21], v[162:165], v[202:205], v[18:21]
	v_mfma_f32_16x16x32_f16 v[14:17], v[162:165], v[210:213], v[14:17]
	v_mfma_f32_16x16x32_f16 v[10:13], v[186:189], v[194:197], v[10:13]
	v_mfma_f32_16x16x32_f16 v[6:9], v[186:189], v[202:205], v[6:9]
	v_mfma_f32_16x16x32_f16 v[2:5], v[186:189], v[210:213], v[2:5]
	v_mfma_f32_16x16x32_f16 v[22:25], v[182:185], v[198:201], v[22:25]
	v_mfma_f32_16x16x32_f16 v[18:21], v[182:185], v[206:209], v[18:21]
	v_mfma_f32_16x16x32_f16 v[14:17], v[182:185], v[214:217], v[14:17]
	v_mfma_f32_16x16x32_f16 v[10:13], v[190:193], v[198:201], v[10:13]
	v_mfma_f32_16x16x32_f16 v[6:9], v[190:193], v[206:209], v[6:9]
	v_mfma_f32_16x16x32_f16 v[2:5], v[190:193], v[214:217], v[2:5]
	s_add_u32 m0, s12, 0x0
	s_barrier
	ds_read_b128 v[162:165], v121 offset:16384
	ds_read_b128 v[182:185], v121 offset:17408
	ds_read_b128 v[186:189], v108 offset:16384
	ds_read_b128 v[190:193], v108 offset:17408
	global_load_lds_dwordx4 v232, s[8:9]
	s_add_u32 m0, s12, 0x2000
	s_nop 0
	global_load_lds_dwordx4 v233, s[8:9]
	s_barrier
	s_waitcnt lgkmcnt(0)
	v_mfma_f32_16x16x32_f16 v[26:29], v[162:165], v[138:141], v[26:29]
	v_mfma_f32_16x16x32_f16 v[30:33], v[162:165], v[146:149], v[30:33]
	v_mfma_f32_16x16x32_f16 v[34:37], v[162:165], v[154:157], v[34:37]
	v_mfma_f32_16x16x32_f16 v[38:41], v[186:189], v[138:141], v[38:41]
	v_mfma_f32_16x16x32_f16 v[46:49], v[186:189], v[146:149], v[46:49]
	v_mfma_f32_16x16x32_f16 v[54:57], v[186:189], v[154:157], v[54:57]
	v_mfma_f32_16x16x32_f16 v[26:29], v[182:185], v[142:145], v[26:29]
	v_mfma_f32_16x16x32_f16 v[30:33], v[182:185], v[150:153], v[30:33]
	v_mfma_f32_16x16x32_f16 v[34:37], v[182:185], v[158:161], v[34:37]
	v_mfma_f32_16x16x32_f16 v[38:41], v[190:193], v[142:145], v[38:41]
	v_mfma_f32_16x16x32_f16 v[46:49], v[190:193], v[150:153], v[46:49]
	v_mfma_f32_16x16x32_f16 v[54:57], v[190:193], v[158:161], v[54:57]
	s_barrier
	s_add_u32 m0, s12, 0x14000
	s_nop 0
	global_load_lds_dwordx4 v244, s[10:11]
	s_add_u32 m0, s12, 0x16000
	s_nop 0
	global_load_lds_dwordx4 v245, s[10:11]
	s_waitcnt vmcnt(6)
	s_barrier
	v_mfma_f32_16x16x32_f16 v[42:45], v[162:165], v[194:197], v[42:45]
	v_mfma_f32_16x16x32_f16 v[50:53], v[162:165], v[202:205], v[50:53]
	v_mfma_f32_16x16x32_f16 v[58:61], v[162:165], v[210:213], v[58:61]
	v_mfma_f32_16x16x32_f16 v[62:65], v[186:189], v[194:197], v[62:65]
	v_mfma_f32_16x16x32_f16 v[70:73], v[186:189], v[202:205], v[70:73]
	v_mfma_f32_16x16x32_f16 v[74:77], v[186:189], v[210:213], v[74:77]
	v_mfma_f32_16x16x32_f16 v[42:45], v[182:185], v[198:201], v[42:45]
	v_mfma_f32_16x16x32_f16 v[50:53], v[182:185], v[206:209], v[50:53]
	v_mfma_f32_16x16x32_f16 v[58:61], v[182:185], v[214:217], v[58:61]
	v_mfma_f32_16x16x32_f16 v[62:65], v[190:193], v[198:201], v[62:65]
	v_mfma_f32_16x16x32_f16 v[70:73], v[190:193], v[206:209], v[70:73]
	v_mfma_f32_16x16x32_f16 v[74:77], v[190:193], v[214:217], v[74:77]
	s_barrier
	ds_read_b128 v[138:141], v127
	ds_read_b128 v[142:145], v127 offset:1024
	ds_read_b128 v[146:149], v127 offset:2048
	ds_read_b128 v[150:153], v127 offset:3072
	ds_read_b128 v[154:157], v127 offset:4096
	ds_read_b128 v[158:161], v127 offset:5120
	s_add_u32 m0, s12, 0x4000
	ds_read_b128 v[162:165], v121 offset:32768
	ds_read_b128 v[182:185], v121 offset:33792
	ds_read_b128 v[186:189], v108 offset:32768
	ds_read_b128 v[190:193], v108 offset:33792
	global_load_lds_dwordx4 v238, s[8:9]
	s_add_u32 m0, s12, 0x6000
	s_nop 0
	global_load_lds_dwordx4 v239, s[8:9]
	s_waitcnt lgkmcnt(4)
	s_barrier
	s_waitcnt lgkmcnt(0)
	v_mfma_f32_16x16x32_f16 v[94:97], v[162:165], v[138:141], v[94:97]
	v_mfma_f32_16x16x32_f16 v[90:93], v[162:165], v[146:149], v[90:93]
	v_mfma_f32_16x16x32_f16 v[86:89], v[162:165], v[154:157], v[86:89]
	v_mfma_f32_16x16x32_f16 v[82:85], v[186:189], v[138:141], v[82:85]
	v_mfma_f32_16x16x32_f16 v[78:81], v[186:189], v[146:149], v[78:81]
	v_mfma_f32_16x16x32_f16 v[66:69], v[186:189], v[154:157], v[66:69]
	v_mfma_f32_16x16x32_f16 v[94:97], v[182:185], v[142:145], v[94:97]
	v_mfma_f32_16x16x32_f16 v[90:93], v[182:185], v[150:153], v[90:93]
	v_mfma_f32_16x16x32_f16 v[86:89], v[182:185], v[158:161], v[86:89]
	v_mfma_f32_16x16x32_f16 v[82:85], v[190:193], v[142:145], v[82:85]
	v_mfma_f32_16x16x32_f16 v[78:81], v[190:193], v[150:153], v[78:81]
	v_mfma_f32_16x16x32_f16 v[66:69], v[190:193], v[158:161], v[66:69]
	s_barrier
	s_add_u32 m0, s12, 0x18000
	ds_read_b128 v[194:197], v124
	ds_read_b128 v[198:201], v124 offset:1024
	ds_read_b128 v[202:205], v124 offset:2048
	ds_read_b128 v[206:209], v124 offset:3072
	ds_read_b128 v[210:213], v124 offset:4096
	ds_read_b128 v[214:217], v124 offset:5120
	global_load_lds_dwordx4 v242, s[10:11]
	s_add_u32 m0, s12, 0x1a000
	s_nop 0
	global_load_lds_dwordx4 v243, s[10:11]
	s_barrier
	s_waitcnt lgkmcnt(0)
	v_mfma_f32_16x16x32_f16 v[22:25], v[162:165], v[194:197], v[22:25]
	v_mfma_f32_16x16x32_f16 v[18:21], v[162:165], v[202:205], v[18:21]
	v_mfma_f32_16x16x32_f16 v[14:17], v[162:165], v[210:213], v[14:17]
	v_mfma_f32_16x16x32_f16 v[10:13], v[186:189], v[194:197], v[10:13]
	v_mfma_f32_16x16x32_f16 v[6:9], v[186:189], v[202:205], v[6:9]
	v_mfma_f32_16x16x32_f16 v[2:5], v[186:189], v[210:213], v[2:5]
	v_mfma_f32_16x16x32_f16 v[22:25], v[182:185], v[198:201], v[22:25]
	v_mfma_f32_16x16x32_f16 v[18:21], v[182:185], v[206:209], v[18:21]
	v_mfma_f32_16x16x32_f16 v[14:17], v[182:185], v[214:217], v[14:17]
	v_mfma_f32_16x16x32_f16 v[10:13], v[190:193], v[198:201], v[10:13]
	v_mfma_f32_16x16x32_f16 v[6:9], v[190:193], v[206:209], v[6:9]
	v_mfma_f32_16x16x32_f16 v[2:5], v[190:193], v[214:217], v[2:5]
	s_add_u32 m0, s12, 0x8000
	s_barrier
	ds_read_b128 v[162:165], v121 offset:49152
	ds_read_b128 v[182:185], v121 offset:50176
	ds_read_b128 v[186:189], v108 offset:49152
	ds_read_b128 v[190:193], v108 offset:50176
	global_load_lds_dwordx4 v234, s[8:9]
	s_add_u32 m0, s12, 0xa000
	s_nop 0
	global_load_lds_dwordx4 v235, s[8:9]
	s_barrier
	s_waitcnt lgkmcnt(0)
	v_mfma_f32_16x16x32_f16 v[26:29], v[162:165], v[138:141], v[26:29]
	v_mfma_f32_16x16x32_f16 v[30:33], v[162:165], v[146:149], v[30:33]
	v_mfma_f32_16x16x32_f16 v[34:37], v[162:165], v[154:157], v[34:37]
	v_mfma_f32_16x16x32_f16 v[38:41], v[186:189], v[138:141], v[38:41]
	v_mfma_f32_16x16x32_f16 v[46:49], v[186:189], v[146:149], v[46:49]
	v_mfma_f32_16x16x32_f16 v[54:57], v[186:189], v[154:157], v[54:57]
	v_mfma_f32_16x16x32_f16 v[26:29], v[182:185], v[142:145], v[26:29]
	v_mfma_f32_16x16x32_f16 v[30:33], v[182:185], v[150:153], v[30:33]
	v_mfma_f32_16x16x32_f16 v[34:37], v[182:185], v[158:161], v[34:37]
	v_mfma_f32_16x16x32_f16 v[38:41], v[190:193], v[142:145], v[38:41]
	v_mfma_f32_16x16x32_f16 v[46:49], v[190:193], v[150:153], v[46:49]
	v_mfma_f32_16x16x32_f16 v[54:57], v[190:193], v[158:161], v[54:57]
	s_barrier
	s_add_u32 m0, s12, 0x1c000
	s_nop 0
	global_load_lds_dwordx4 v246, s[10:11]
	s_add_u32 m0, s12, 0x1e000
	s_nop 0
	global_load_lds_dwordx4 v247, s[10:11]
	s_waitcnt vmcnt(6)
	s_barrier
	v_mfma_f32_16x16x32_f16 v[42:45], v[162:165], v[194:197], v[42:45]
	v_mfma_f32_16x16x32_f16 v[50:53], v[162:165], v[202:205], v[50:53]
	v_mfma_f32_16x16x32_f16 v[58:61], v[162:165], v[210:213], v[58:61]
	v_mfma_f32_16x16x32_f16 v[62:65], v[186:189], v[194:197], v[62:65]
	v_mfma_f32_16x16x32_f16 v[70:73], v[186:189], v[202:205], v[70:73]
	v_mfma_f32_16x16x32_f16 v[74:77], v[186:189], v[210:213], v[74:77]
	v_mfma_f32_16x16x32_f16 v[42:45], v[182:185], v[198:201], v[42:45]
	v_mfma_f32_16x16x32_f16 v[50:53], v[182:185], v[206:209], v[50:53]
	v_mfma_f32_16x16x32_f16 v[58:61], v[182:185], v[214:217], v[58:61]
	v_mfma_f32_16x16x32_f16 v[62:65], v[190:193], v[198:201], v[62:65]
	v_mfma_f32_16x16x32_f16 v[70:73], v[190:193], v[206:209], v[70:73]
	v_mfma_f32_16x16x32_f16 v[74:77], v[190:193], v[214:217], v[74:77]
	s_add_i32 s4, s4, 2
	s_add_u32 s2, s2, 0x100
	s_addc_u32 s3, s3, 0
	s_add_u32 s8, s8, 0x100
	s_addc_u32 s9, s9, 0
	s_add_u32 s10, s10, 0x100
	s_addc_u32 s11, s11, 0
	s_cmp_lt_u32 s4, 8
	s_barrier
	s_cbranch_scc1 .LBB1_52
	s_mov_b64 s[4:5], 0x580
	v_readfirstlane_b32 s2, v136
	v_lshl_add_u64 v[98:99], v[98:99], 0, s[4:5]
	s_mov_b32 m0, s2
	v_readfirstlane_b32 s2, v137
	ds_read_b128 v[102:105], v135
	ds_read_b128 v[110:113], v135 offset:1024
	ds_read_b128 v[114:117], v135 offset:2048
	ds_read_b128 v[128:131], v135 offset:3072
	ds_read_b128 v[138:141], v135 offset:4096
	ds_read_b128 v[142:145], v135 offset:5120
	ds_read_b128 v[146:149], v121
	ds_read_b128 v[150:153], v121 offset:1024
	ds_read_b128 v[154:157], v108
	ds_read_b128 v[158:161], v108 offset:1024
	global_load_lds_dwordx4 v[98:99], off
	v_lshl_add_u64 v[98:99], v[100:101], 0, s[4:5]
	s_mov_b32 m0, s2
	s_nop 0
	global_load_lds_dwordx4 v[98:99], off
	s_barrier
	s_waitcnt lgkmcnt(0)
	s_setprio 1
	s_waitcnt lgkmcnt(0)
	v_mfma_f32_16x16x32_f16 v[94:97], v[146:149], v[102:105], v[94:97]
	v_mfma_f32_16x16x32_f16 v[90:93], v[146:149], v[114:117], v[90:93]
	v_mfma_f32_16x16x32_f16 v[86:89], v[146:149], v[138:141], v[86:89]
	v_mfma_f32_16x16x32_f16 v[82:85], v[154:157], v[102:105], v[82:85]
	v_mfma_f32_16x16x32_f16 v[78:81], v[154:157], v[114:117], v[78:81]
	v_mfma_f32_16x16x32_f16 v[66:69], v[154:157], v[138:141], v[66:69]
	v_mfma_f32_16x16x32_f16 v[94:97], v[150:153], v[110:113], v[94:97]
	v_mfma_f32_16x16x32_f16 v[90:93], v[150:153], v[128:131], v[90:93]
	v_mfma_f32_16x16x32_f16 v[86:89], v[150:153], v[142:145], v[86:89]
	v_mfma_f32_16x16x32_f16 v[82:85], v[158:161], v[110:113], v[82:85]
	v_mfma_f32_16x16x32_f16 v[98:101], v[158:161], v[128:131], v[78:81]
	v_mfma_f32_16x16x32_f16 v[66:69], v[158:161], v[142:145], v[66:69]
	s_setprio 0
	s_barrier
	ds_read_b128 v[78:81], v134
	ds_read_b128 v[162:165], v134 offset:1024
	ds_read_b128 v[182:185], v134 offset:2048
	ds_read_b128 v[186:189], v134 offset:3072
	ds_read_b128 v[190:193], v134 offset:4096
	ds_read_b128 v[132:135], v134 offset:5120
	s_barrier
	s_waitcnt lgkmcnt(0)
	s_setprio 1
	s_waitcnt lgkmcnt(0)
	v_mfma_f32_16x16x32_f16 v[22:25], v[146:149], v[78:81], v[22:25]
	v_mfma_f32_16x16x32_f16 v[18:21], v[146:149], v[182:185], v[18:21]
	v_mfma_f32_16x16x32_f16 v[14:17], v[146:149], v[190:193], v[14:17]
	v_mfma_f32_16x16x32_f16 v[10:13], v[154:157], v[78:81], v[10:13]
	v_mfma_f32_16x16x32_f16 v[6:9], v[154:157], v[182:185], v[6:9]
	v_mfma_f32_16x16x32_f16 v[2:5], v[154:157], v[190:193], v[2:5]
	v_mfma_f32_16x16x32_f16 v[22:25], v[150:153], v[162:165], v[22:25]
	v_mfma_f32_16x16x32_f16 v[18:21], v[150:153], v[186:189], v[18:21]
	v_mfma_f32_16x16x32_f16 v[14:17], v[150:153], v[132:135], v[14:17]
	v_mfma_f32_16x16x32_f16 v[10:13], v[158:161], v[162:165], v[10:13]
	v_mfma_f32_16x16x32_f16 v[6:9], v[158:161], v[186:189], v[6:9]
	v_mfma_f32_16x16x32_f16 v[2:5], v[158:161], v[132:135], v[2:5]
	s_setprio 0
	s_barrier
	ds_read_b128 v[146:149], v121 offset:16384
	ds_read_b128 v[150:153], v121 offset:17408
	ds_read_b128 v[154:157], v108 offset:16384
	ds_read_b128 v[158:161], v108 offset:17408
	s_waitcnt vmcnt(4)
	s_barrier
	s_waitcnt lgkmcnt(0)
	s_setprio 1
	s_waitcnt lgkmcnt(0)
	v_mfma_f32_16x16x32_f16 v[26:29], v[146:149], v[102:105], v[26:29]
	v_mfma_f32_16x16x32_f16 v[30:33], v[146:149], v[114:117], v[30:33]
	v_mfma_f32_16x16x32_f16 v[34:37], v[146:149], v[138:141], v[34:37]
	v_mfma_f32_16x16x32_f16 v[38:41], v[154:157], v[102:105], v[38:41]
	v_mfma_f32_16x16x32_f16 v[46:49], v[154:157], v[114:117], v[46:49]
	v_mfma_f32_16x16x32_f16 v[26:29], v[150:153], v[110:113], v[26:29]
	v_mfma_f32_16x16x32_f16 v[30:33], v[150:153], v[128:131], v[30:33]
	v_mfma_f32_16x16x32_f16 v[34:37], v[150:153], v[142:145], v[34:37]
	v_mfma_f32_16x16x32_f16 v[38:41], v[158:161], v[110:113], v[38:41]
	v_mfma_f32_16x16x32_f16 v[46:49], v[158:161], v[128:131], v[46:49]
	v_mfma_f32_16x16x32_f16 v[54:57], v[154:157], v[138:141], v[54:57]
	v_mfma_f32_16x16x32_f16 v[54:57], v[158:161], v[142:145], v[54:57]
	s_setprio 0
	s_setprio 1
	v_mfma_f32_16x16x32_f16 v[58:61], v[146:149], v[190:193], v[58:61]
	v_mfma_f32_16x16x32_f16 v[110:113], v[150:153], v[132:135], v[58:61]
	v_mfma_f32_16x16x32_f16 v[58:61], v[154:157], v[78:81], v[62:65]
	v_mfma_f32_16x16x32_f16 v[42:45], v[146:149], v[78:81], v[42:45]
	v_mfma_f32_16x16x32_f16 v[114:117], v[158:161], v[162:165], v[58:61]
	v_mfma_f32_16x16x32_f16 v[58:61], v[154:157], v[182:185], v[70:73]
	v_mfma_f32_16x16x32_f16 v[42:45], v[150:153], v[162:165], v[42:45]
	v_mfma_f32_16x16x32_f16 v[50:53], v[146:149], v[182:185], v[50:53]
	v_mfma_f32_16x16x32_f16 v[128:131], v[158:161], v[186:189], v[58:61]
	v_mfma_f32_16x16x32_f16 v[58:61], v[154:157], v[190:193], v[74:77]
	v_mfma_f32_16x16x32_f16 v[50:53], v[150:153], v[186:189], v[50:53]
	v_mfma_f32_16x16x32_f16 v[132:135], v[158:161], v[132:135], v[58:61]
	s_setprio 0
	s_barrier
	ds_read_b128 v[136:139], v127
	ds_read_b128 v[140:143], v127 offset:1024
	ds_read_b128 v[144:147], v127 offset:2048
	ds_read_b128 v[148:151], v127 offset:3072
	ds_read_b128 v[152:155], v127 offset:4096
	ds_read_b128 v[156:159], v127 offset:5120
	ds_read_b128 v[74:77], v121 offset:32768
	ds_read_b128 v[160:163], v121 offset:33792
	ds_read_b128 v[164:167], v108 offset:32768
	ds_read_b128 v[182:185], v108 offset:33792
	s_waitcnt vmcnt(2)
	s_barrier
	s_waitcnt lgkmcnt(0)
	s_setprio 1
	s_waitcnt lgkmcnt(0)
	v_mfma_f32_16x16x32_f16 v[62:65], v[74:77], v[144:147], v[90:93]
	v_mfma_f32_16x16x32_f16 v[70:73], v[164:167], v[136:139], v[82:85]
	v_mfma_f32_16x16x32_f16 v[58:61], v[74:77], v[136:139], v[94:97]
	v_mfma_f32_16x16x32_f16 v[78:81], v[160:163], v[148:151], v[62:65]
	v_mfma_f32_16x16x32_f16 v[62:65], v[74:77], v[152:155], v[86:89]
	v_mfma_f32_16x16x32_f16 v[102:105], v[182:185], v[140:143], v[70:73]
	v_mfma_f32_16x16x32_f16 v[70:73], v[164:167], v[144:147], v[98:101]
	v_mfma_f32_16x16x32_f16 v[66:69], v[164:167], v[152:155], v[66:69]
	v_mfma_f32_16x16x32_f16 v[58:61], v[160:163], v[140:143], v[58:61]
	v_mfma_f32_16x16x32_f16 v[62:65], v[160:163], v[156:159], v[62:65]
	v_mfma_f32_16x16x32_f16 v[86:89], v[182:185], v[148:151], v[70:73]
	v_mfma_f32_16x16x32_f16 v[70:73], v[182:185], v[156:159], v[66:69]
	s_setprio 0
	s_barrier
	ds_read_b128 v[186:189], v124
	ds_read_b128 v[190:193], v124 offset:1024
	ds_read_b128 v[194:197], v124 offset:2048
	ds_read_b128 v[198:201], v124 offset:3072
	ds_read_b128 v[202:205], v124 offset:4096
	ds_read_b128 v[122:125], v124 offset:5120
	s_waitcnt vmcnt(0)
	s_barrier
	s_waitcnt lgkmcnt(0)
	s_setprio 1
	s_waitcnt lgkmcnt(0)
	v_mfma_f32_16x16x32_f16 v[22:25], v[74:77], v[186:189], v[22:25]
	v_mfma_f32_16x16x32_f16 v[18:21], v[74:77], v[194:197], v[18:21]
	v_mfma_f32_16x16x32_f16 v[14:17], v[74:77], v[202:205], v[14:17]
	v_mfma_f32_16x16x32_f16 v[10:13], v[164:167], v[186:189], v[10:13]
	v_mfma_f32_16x16x32_f16 v[6:9], v[164:167], v[194:197], v[6:9]
	v_mfma_f32_16x16x32_f16 v[2:5], v[164:167], v[202:205], v[2:5]
	v_mfma_f32_16x16x32_f16 v[94:97], v[160:163], v[190:193], v[22:25]
	v_mfma_f32_16x16x32_f16 v[82:85], v[160:163], v[198:201], v[18:21]
	v_mfma_f32_16x16x32_f16 v[66:69], v[160:163], v[122:125], v[14:17]
	v_mfma_f32_16x16x32_f16 v[98:101], v[182:185], v[190:193], v[10:13]
	v_mfma_f32_16x16x32_f16 v[90:93], v[182:185], v[198:201], v[6:9]
	v_mfma_f32_16x16x32_f16 v[74:77], v[182:185], v[122:125], v[2:5]
	s_setprio 0
	s_barrier
	ds_read_b128 v[10:13], v121 offset:49152
	ds_read_b128 v[160:163], v121 offset:50176
	ds_read_b128 v[164:167], v108 offset:49152
	ds_read_b128 v[182:185], v108 offset:50176
	s_barrier
	s_waitcnt lgkmcnt(0)
	s_setprio 1
	s_waitcnt lgkmcnt(0)
	v_mfma_f32_16x16x32_f16 v[2:5], v[10:13], v[136:139], v[26:29]
	v_mfma_f32_16x16x32_f16 v[18:21], v[164:167], v[136:139], v[38:41]
	v_mfma_f32_16x16x32_f16 v[14:17], v[160:163], v[140:143], v[2:5]
	v_mfma_f32_16x16x32_f16 v[2:5], v[10:13], v[144:147], v[30:33]
	v_mfma_f32_16x16x32_f16 v[38:41], v[182:185], v[140:143], v[18:21]
	v_mfma_f32_16x16x32_f16 v[18:21], v[164:167], v[144:147], v[46:49]
	v_mfma_f32_16x16x32_f16 v[6:9], v[160:163], v[148:151], v[2:5]
	v_mfma_f32_16x16x32_f16 v[2:5], v[10:13], v[152:155], v[34:37]
	v_mfma_f32_16x16x32_f16 v[26:29], v[182:185], v[148:151], v[18:21]
	v_mfma_f32_16x16x32_f16 v[18:21], v[164:167], v[152:155], v[54:57]
	v_mfma_f32_16x16x32_f16 v[2:5], v[160:163], v[156:159], v[2:5]
	v_mfma_f32_16x16x32_f16 v[18:21], v[182:185], v[156:159], v[18:21]
	s_setprio 0
	s_setprio 1
	v_mfma_f32_16x16x32_f16 v[34:37], v[164:167], v[186:189], v[114:117]
	v_mfma_f32_16x16x32_f16 v[22:25], v[10:13], v[186:189], v[42:45]
	v_mfma_f32_16x16x32_f16 v[46:49], v[182:185], v[190:193], v[34:37]
	v_mfma_f32_16x16x32_f16 v[34:37], v[164:167], v[194:197], v[128:131]
	v_mfma_f32_16x16x32_f16 v[30:33], v[160:163], v[190:193], v[22:25]
	v_mfma_f32_16x16x32_f16 v[22:25], v[10:13], v[194:197], v[50:53]
	v_mfma_f32_16x16x32_f16 v[10:13], v[10:13], v[202:205], v[110:113]
	v_mfma_f32_16x16x32_f16 v[42:45], v[182:185], v[198:201], v[34:37]
	v_mfma_f32_16x16x32_f16 v[34:37], v[164:167], v[202:205], v[132:135]
	v_mfma_f32_16x16x32_f16 v[22:25], v[160:163], v[198:201], v[22:25]
	v_mfma_f32_16x16x32_f16 v[10:13], v[160:163], v[122:125], v[10:13]
	v_mfma_f32_16x16x32_f16 v[34:37], v[182:185], v[122:125], v[34:37]
	s_setprio 0
	s_movk_i32 s2, 0x100
	v_cmp_gt_u32_e32 vcc, s2, v175
	s_barrier
	s_and_saveexec_b64 s[2:3], vcc
	s_cbranch_execz .LBB1_55
	s_barrier

.LBB1_66:
	ds_read_b128 v[148:151], v144
	ds_read_b128 v[152:155], v144 offset:1024
	ds_read_b128 v[156:159], v144 offset:2048
	ds_read_b128 v[160:163], v144 offset:3072
	ds_read_b128 v[164:167], v144 offset:4096
	ds_read_b128 v[174:177], v144 offset:5120
	s_add_u32 m0, s12, 0xc000
	ds_read_b128 v[178:181], v130
	ds_read_b128 v[182:185], v130 offset:1024
	ds_read_b128 v[186:189], v108
	ds_read_b128 v[190:193], v108 offset:1024
	global_load_lds_dwordx4 v236, s[8:9]
	s_add_u32 m0, s12, 0xe000
	s_nop 0
	global_load_lds_dwordx4 v237, s[8:9]
	s_waitcnt lgkmcnt(4)
	s_barrier
	s_waitcnt lgkmcnt(0)
	v_mfma_f32_16x16x32_f16 v[94:97], v[178:181], v[148:151], v[94:97]
	v_mfma_f32_16x16x32_f16 v[90:93], v[178:181], v[156:159], v[90:93]
	v_mfma_f32_16x16x32_f16 v[86:89], v[178:181], v[164:167], v[86:89]
	v_mfma_f32_16x16x32_f16 v[74:77], v[186:189], v[148:151], v[74:77]
	v_mfma_f32_16x16x32_f16 v[46:49], v[186:189], v[156:159], v[46:49]
	v_mfma_f32_16x16x32_f16 v[18:21], v[186:189], v[164:167], v[18:21]
	v_mfma_f32_16x16x32_f16 v[94:97], v[182:185], v[152:155], v[94:97]
	v_mfma_f32_16x16x32_f16 v[90:93], v[182:185], v[160:163], v[90:93]
	v_mfma_f32_16x16x32_f16 v[86:89], v[182:185], v[174:177], v[86:89]
	v_mfma_f32_16x16x32_f16 v[74:77], v[190:193], v[152:155], v[74:77]
	v_mfma_f32_16x16x32_f16 v[46:49], v[190:193], v[160:163], v[46:49]
	v_mfma_f32_16x16x32_f16 v[18:21], v[190:193], v[174:177], v[18:21]
	s_barrier
	s_add_u32 m0, s12, 0x10000
	ds_read_b128 v[194:197], v143
	ds_read_b128 v[198:201], v143 offset:1024
	ds_read_b128 v[202:205], v143 offset:2048
	ds_read_b128 v[206:209], v143 offset:3072
	ds_read_b128 v[210:213], v143 offset:4096
	ds_read_b128 v[214:217], v143 offset:5120
	global_load_lds_dwordx4 v240, s[10:11]
	s_add_u32 m0, s12, 0x12000
	s_nop 0
	global_load_lds_dwordx4 v241, s[10:11]
	s_barrier
	s_waitcnt lgkmcnt(0)
	v_mfma_f32_16x16x32_f16 v[10:13], v[178:181], v[194:197], v[10:13]
	v_mfma_f32_16x16x32_f16 v[6:9], v[178:181], v[202:205], v[6:9]
	v_mfma_f32_16x16x32_f16 v[2:5], v[178:181], v[210:213], v[2:5]
	v_mfma_f32_16x16x32_f16 v[26:29], v[186:189], v[194:197], v[26:29]
	v_mfma_f32_16x16x32_f16 v[34:37], v[186:189], v[202:205], v[34:37]
	v_mfma_f32_16x16x32_f16 v[50:53], v[186:189], v[210:213], v[50:53]
	v_mfma_f32_16x16x32_f16 v[10:13], v[182:185], v[198:201], v[10:13]
	v_mfma_f32_16x16x32_f16 v[6:9], v[182:185], v[206:209], v[6:9]
	v_mfma_f32_16x16x32_f16 v[2:5], v[182:185], v[214:217], v[2:5]
	v_mfma_f32_16x16x32_f16 v[26:29], v[190:193], v[198:201], v[26:29]
	v_mfma_f32_16x16x32_f16 v[34:37], v[190:193], v[206:209], v[34:37]
	v_mfma_f32_16x16x32_f16 v[50:53], v[190:193], v[214:217], v[50:53]
	s_add_u32 m0, s12, 0x0
	s_barrier
	ds_read_b128 v[178:181], v130 offset:16384
	ds_read_b128 v[182:185], v130 offset:17408
	ds_read_b128 v[186:189], v108 offset:16384
	ds_read_b128 v[190:193], v108 offset:17408
	global_load_lds_dwordx4 v232, s[8:9]
	s_add_u32 m0, s12, 0x2000
	s_nop 0
	global_load_lds_dwordx4 v233, s[8:9]
	s_barrier
	s_waitcnt lgkmcnt(0)
	v_mfma_f32_16x16x32_f16 v[14:17], v[178:181], v[148:151], v[14:17]
	v_mfma_f32_16x16x32_f16 v[22:25], v[178:181], v[156:159], v[22:25]
	v_mfma_f32_16x16x32_f16 v[30:33], v[178:181], v[164:167], v[30:33]
	v_mfma_f32_16x16x32_f16 v[38:41], v[186:189], v[148:151], v[38:41]
	v_mfma_f32_16x16x32_f16 v[54:57], v[186:189], v[156:159], v[54:57]
	v_mfma_f32_16x16x32_f16 v[62:65], v[186:189], v[164:167], v[62:65]
	v_mfma_f32_16x16x32_f16 v[14:17], v[182:185], v[152:155], v[14:17]
	v_mfma_f32_16x16x32_f16 v[22:25], v[182:185], v[160:163], v[22:25]
	v_mfma_f32_16x16x32_f16 v[30:33], v[182:185], v[174:177], v[30:33]
	v_mfma_f32_16x16x32_f16 v[38:41], v[190:193], v[152:155], v[38:41]
	v_mfma_f32_16x16x32_f16 v[54:57], v[190:193], v[160:163], v[54:57]
	v_mfma_f32_16x16x32_f16 v[62:65], v[190:193], v[174:177], v[62:65]
	s_barrier
	s_add_u32 m0, s12, 0x14000
	s_nop 0
	global_load_lds_dwordx4 v244, s[10:11]
	s_add_u32 m0, s12, 0x16000
	s_nop 0
	global_load_lds_dwordx4 v245, s[10:11]
	s_waitcnt vmcnt(6)
	s_barrier
	v_mfma_f32_16x16x32_f16 v[42:45], v[178:181], v[194:197], v[42:45]
	v_mfma_f32_16x16x32_f16 v[58:61], v[178:181], v[202:205], v[58:61]
	v_mfma_f32_16x16x32_f16 v[66:69], v[178:181], v[210:213], v[66:69]
	v_mfma_f32_16x16x32_f16 v[70:73], v[186:189], v[194:197], v[70:73]
	v_mfma_f32_16x16x32_f16 v[78:81], v[186:189], v[202:205], v[78:81]
	v_mfma_f32_16x16x32_f16 v[82:85], v[186:189], v[210:213], v[82:85]
	v_mfma_f32_16x16x32_f16 v[42:45], v[182:185], v[198:201], v[42:45]
	v_mfma_f32_16x16x32_f16 v[58:61], v[182:185], v[206:209], v[58:61]
	v_mfma_f32_16x16x32_f16 v[66:69], v[182:185], v[214:217], v[66:69]
	v_mfma_f32_16x16x32_f16 v[70:73], v[190:193], v[198:201], v[70:73]
	v_mfma_f32_16x16x32_f16 v[78:81], v[190:193], v[206:209], v[78:81]
	v_mfma_f32_16x16x32_f16 v[82:85], v[190:193], v[214:217], v[82:85]
	s_barrier
	ds_read_b128 v[148:151], v136
	ds_read_b128 v[152:155], v136 offset:1024
	ds_read_b128 v[156:159], v136 offset:2048
	ds_read_b128 v[160:163], v136 offset:3072
	ds_read_b128 v[164:167], v136 offset:4096
	ds_read_b128 v[174:177], v136 offset:5120
	s_add_u32 m0, s12, 0x4000
	ds_read_b128 v[178:181], v130 offset:32768
	ds_read_b128 v[182:185], v130 offset:33792
	ds_read_b128 v[186:189], v108 offset:32768
	ds_read_b128 v[190:193], v108 offset:33792
	global_load_lds_dwordx4 v238, s[8:9]
	s_add_u32 m0, s12, 0x6000
	s_nop 0
	global_load_lds_dwordx4 v239, s[8:9]
	s_waitcnt lgkmcnt(4)
	s_barrier
	s_waitcnt lgkmcnt(0)
	v_mfma_f32_16x16x32_f16 v[94:97], v[178:181], v[148:151], v[94:97]
	v_mfma_f32_16x16x32_f16 v[90:93], v[178:181], v[156:159], v[90:93]
	v_mfma_f32_16x16x32_f16 v[86:89], v[178:181], v[164:167], v[86:89]
	v_mfma_f32_16x16x32_f16 v[74:77], v[186:189], v[148:151], v[74:77]
	v_mfma_f32_16x16x32_f16 v[46:49], v[186:189], v[156:159], v[46:49]
	v_mfma_f32_16x16x32_f16 v[18:21], v[186:189], v[164:167], v[18:21]
	v_mfma_f32_16x16x32_f16 v[94:97], v[182:185], v[152:155], v[94:97]
	v_mfma_f32_16x16x32_f16 v[90:93], v[182:185], v[160:163], v[90:93]
	v_mfma_f32_16x16x32_f16 v[86:89], v[182:185], v[174:177], v[86:89]
	v_mfma_f32_16x16x32_f16 v[74:77], v[190:193], v[152:155], v[74:77]
	v_mfma_f32_16x16x32_f16 v[46:49], v[190:193], v[160:163], v[46:49]
	v_mfma_f32_16x16x32_f16 v[18:21], v[190:193], v[174:177], v[18:21]
	s_barrier
	s_add_u32 m0, s12, 0x18000
	ds_read_b128 v[194:197], v133
	ds_read_b128 v[198:201], v133 offset:1024
	ds_read_b128 v[202:205], v133 offset:2048
	ds_read_b128 v[206:209], v133 offset:3072
	ds_read_b128 v[210:213], v133 offset:4096
	ds_read_b128 v[214:217], v133 offset:5120
	global_load_lds_dwordx4 v242, s[10:11]
	s_add_u32 m0, s12, 0x1a000
	s_nop 0
	global_load_lds_dwordx4 v243, s[10:11]
	s_barrier
	s_waitcnt lgkmcnt(0)
	v_mfma_f32_16x16x32_f16 v[10:13], v[178:181], v[194:197], v[10:13]
	v_mfma_f32_16x16x32_f16 v[6:9], v[178:181], v[202:205], v[6:9]
	v_mfma_f32_16x16x32_f16 v[2:5], v[178:181], v[210:213], v[2:5]
	v_mfma_f32_16x16x32_f16 v[26:29], v[186:189], v[194:197], v[26:29]
	v_mfma_f32_16x16x32_f16 v[34:37], v[186:189], v[202:205], v[34:37]
	v_mfma_f32_16x16x32_f16 v[50:53], v[186:189], v[210:213], v[50:53]
	v_mfma_f32_16x16x32_f16 v[10:13], v[182:185], v[198:201], v[10:13]
	v_mfma_f32_16x16x32_f16 v[6:9], v[182:185], v[206:209], v[6:9]
	v_mfma_f32_16x16x32_f16 v[2:5], v[182:185], v[214:217], v[2:5]
	v_mfma_f32_16x16x32_f16 v[26:29], v[190:193], v[198:201], v[26:29]
	v_mfma_f32_16x16x32_f16 v[34:37], v[190:193], v[206:209], v[34:37]
	v_mfma_f32_16x16x32_f16 v[50:53], v[190:193], v[214:217], v[50:53]
	s_add_u32 m0, s12, 0x8000
	s_barrier
	ds_read_b128 v[178:181], v130 offset:49152
	ds_read_b128 v[182:185], v130 offset:50176
	ds_read_b128 v[186:189], v108 offset:49152
	ds_read_b128 v[190:193], v108 offset:50176
	global_load_lds_dwordx4 v234, s[8:9]
	s_add_u32 m0, s12, 0xa000
	s_nop 0
	global_load_lds_dwordx4 v235, s[8:9]
	s_barrier
	s_waitcnt lgkmcnt(0)
	v_mfma_f32_16x16x32_f16 v[14:17], v[178:181], v[148:151], v[14:17]
	v_mfma_f32_16x16x32_f16 v[22:25], v[178:181], v[156:159], v[22:25]
	v_mfma_f32_16x16x32_f16 v[30:33], v[178:181], v[164:167], v[30:33]
	v_mfma_f32_16x16x32_f16 v[38:41], v[186:189], v[148:151], v[38:41]
	v_mfma_f32_16x16x32_f16 v[54:57], v[186:189], v[156:159], v[54:57]
	v_mfma_f32_16x16x32_f16 v[62:65], v[186:189], v[164:167], v[62:65]
	v_mfma_f32_16x16x32_f16 v[14:17], v[182:185], v[152:155], v[14:17]
	v_mfma_f32_16x16x32_f16 v[22:25], v[182:185], v[160:163], v[22:25]
	v_mfma_f32_16x16x32_f16 v[30:33], v[182:185], v[174:177], v[30:33]
	v_mfma_f32_16x16x32_f16 v[38:41], v[190:193], v[152:155], v[38:41]
	v_mfma_f32_16x16x32_f16 v[54:57], v[190:193], v[160:163], v[54:57]
	v_mfma_f32_16x16x32_f16 v[62:65], v[190:193], v[174:177], v[62:65]
	s_barrier
	s_add_u32 m0, s12, 0x1c000
	s_nop 0
	global_load_lds_dwordx4 v246, s[10:11]
	s_add_u32 m0, s12, 0x1e000
	s_nop 0
	global_load_lds_dwordx4 v247, s[10:11]
	s_waitcnt vmcnt(6)
	s_barrier
	v_mfma_f32_16x16x32_f16 v[42:45], v[178:181], v[194:197], v[42:45]
	v_mfma_f32_16x16x32_f16 v[58:61], v[178:181], v[202:205], v[58:61]
	v_mfma_f32_16x16x32_f16 v[66:69], v[178:181], v[210:213], v[66:69]
	v_mfma_f32_16x16x32_f16 v[70:73], v[186:189], v[194:197], v[70:73]
	v_mfma_f32_16x16x32_f16 v[78:81], v[186:189], v[202:205], v[78:81]
	v_mfma_f32_16x16x32_f16 v[82:85], v[186:189], v[210:213], v[82:85]
	v_mfma_f32_16x16x32_f16 v[42:45], v[182:185], v[198:201], v[42:45]
	v_mfma_f32_16x16x32_f16 v[58:61], v[182:185], v[206:209], v[58:61]
	v_mfma_f32_16x16x32_f16 v[66:69], v[182:185], v[214:217], v[66:69]
	v_mfma_f32_16x16x32_f16 v[70:73], v[190:193], v[198:201], v[70:73]
	v_mfma_f32_16x16x32_f16 v[78:81], v[190:193], v[206:209], v[78:81]
	v_mfma_f32_16x16x32_f16 v[82:85], v[190:193], v[214:217], v[82:85]
	s_add_i32 s2, s2, 2
	s_add_u32 s0, s0, 0x100
	s_addc_u32 s1, s1, 0
	s_add_u32 s8, s8, 0x100
	s_addc_u32 s9, s9, 0
	s_add_u32 s10, s10, 0x100
	s_addc_u32 s11, s11, 0
	s_cmp_lt_u32 s2, 8
	s_barrier
	s_cbranch_scc1 .LBB1_66
	v_readlane_b32 s10, v230, 2
	v_readlane_b32 s11, v230, 3
	v_or_b32_e32 v238, v126, v125
	v_add_u32_e32 v238, v238, v121
	v_lshlrev_b32_e32 v232, 1, v238
	v_and_b32_e32 v232, -4, v232
	v_add_u32_e32 v233, 16, v238
	v_lshlrev_b32_e32 v233, 1, v233
	v_and_b32_e32 v233, -4, v233
	v_add_u32_e32 v234, 32, v238
	v_lshlrev_b32_e32 v234, 1, v234
	v_and_b32_e32 v234, -4, v234
	v_add_u32_e32 v235, 0x60, v238
	v_lshlrev_b32_e32 v235, 1, v235
	v_and_b32_e32 v235, -4, v235
	v_add_u32_e32 v236, 0x70, v238
	v_lshlrev_b32_e32 v236, 1, v236
	v_and_b32_e32 v236, -4, v236
	v_add_u32_e32 v237, 0x80, v238
	v_lshlrev_b32_e32 v237, 1, v237
	v_and_b32_e32 v237, -4, v237
	global_load_dword v232, v232, s[48:49]
	global_load_dword v233, v233, s[48:49]
	global_load_dword v234, v234, s[48:49]
	global_load_dword v235, v235, s[48:49]
	global_load_dword v236, v236, s[48:49]
	global_load_dword v237, v237, s[48:49]
	s_mov_b32 s32, 0x2aaaaaab
	v_mul_hi_u32 v239, v107, s32
	v_lshrrev_b32_e32 v239, 4, v239
	v_mul_u32_u24_e32 v239, 0x60, v239
	v_sub_u32_e32 v239, v107, v239
	v_lshrrev_b32_e32 v240, 1, v121
	v_add_u32_e32 v239, v239, v240
	v_lshlrev_b32_e32 v239, 3, v239
	global_load_dwordx2 v[240:241], v239, s[10:11]
	global_load_dwordx2 v[242:243], v239, s[10:11] offset:3072
	s_mov_b64 s[2:3], 0x580
	v_readfirstlane_b32 s0, v145
	v_lshl_add_u64 v[100:101], v[100:101], 0, s[2:3]
	s_mov_b32 m0, s0
	v_readfirstlane_b32 s0, v146
	ds_read_b128 v[110:113], v144
	ds_read_b128 v[114:117], v144 offset:1024
	ds_read_b128 v[138:141], v144 offset:2048
	ds_read_b128 v[148:151], v144 offset:3072
	ds_read_b128 v[152:155], v144 offset:4096
	ds_read_b128 v[156:159], v144 offset:5120
	ds_read_b128 v[160:163], v130
	ds_read_b128 v[164:167], v130 offset:1024
	ds_read_b128 v[174:177], v108
	ds_read_b128 v[178:181], v108 offset:1024
	global_load_lds_dwordx4 v[100:101], off
	v_lshl_add_u64 v[100:101], v[102:103], 0, s[2:3]
	s_mov_b32 m0, s0
	s_nop 0
	global_load_lds_dwordx4 v[100:101], off
	s_barrier
	s_waitcnt lgkmcnt(0)
	s_setprio 1
	s_waitcnt lgkmcnt(0)
	v_mfma_f32_16x16x32_f16 v[94:97], v[160:163], v[110:113], v[94:97]
	v_mfma_f32_16x16x32_f16 v[90:93], v[160:163], v[138:141], v[90:93]
	v_mfma_f32_16x16x32_f16 v[86:89], v[160:163], v[152:155], v[86:89]
	v_mfma_f32_16x16x32_f16 v[74:77], v[174:177], v[110:113], v[74:77]
	v_mfma_f32_16x16x32_f16 v[18:21], v[174:177], v[152:155], v[18:21]
	v_mfma_f32_16x16x32_f16 v[94:97], v[164:167], v[114:117], v[94:97]
	v_mfma_f32_16x16x32_f16 v[90:93], v[164:167], v[148:151], v[90:93]
	v_mfma_f32_16x16x32_f16 v[86:89], v[164:167], v[156:159], v[86:89]
	v_mfma_f32_16x16x32_f16 v[74:77], v[178:181], v[114:117], v[74:77]
	v_mfma_f32_16x16x32_f16 v[46:49], v[174:177], v[138:141], v[46:49]
	v_mfma_f32_16x16x32_f16 v[18:21], v[178:181], v[156:159], v[18:21]
	v_mfma_f32_16x16x32_f16 v[100:103], v[178:181], v[148:151], v[46:49]
	s_setprio 0
	s_barrier
	s_nop 3
	ds_read_b128 v[46:49], v143
	ds_read_b128 v[144:147], v143 offset:1024
	ds_read_b128 v[182:185], v143 offset:2048
	ds_read_b128 v[186:189], v143 offset:3072
	ds_read_b128 v[190:193], v143 offset:4096
	ds_read_b128 v[194:197], v143 offset:5120
	s_barrier
	s_waitcnt lgkmcnt(0)
	s_setprio 1
	s_waitcnt lgkmcnt(0)
	v_mfma_f32_16x16x32_f16 v[34:37], v[174:177], v[182:185], v[34:37]
	v_mfma_f32_16x16x32_f16 v[10:13], v[160:163], v[46:49], v[10:13]
	v_mfma_f32_16x16x32_f16 v[6:9], v[160:163], v[182:185], v[6:9]
	v_mfma_f32_16x16x32_f16 v[2:5], v[160:163], v[190:193], v[2:5]
	v_mfma_f32_16x16x32_f16 v[26:29], v[174:177], v[46:49], v[26:29]
	v_mfma_f32_16x16x32_f16 v[160:163], v[178:181], v[186:189], v[34:37]
	v_mfma_f32_16x16x32_f16 v[34:37], v[174:177], v[190:193], v[50:53]
	v_mfma_f32_16x16x32_f16 v[10:13], v[164:167], v[144:147], v[10:13]
	v_mfma_f32_16x16x32_f16 v[6:9], v[164:167], v[186:189], v[6:9]
	v_mfma_f32_16x16x32_f16 v[2:5], v[164:167], v[194:197], v[2:5]
	v_mfma_f32_16x16x32_f16 v[26:29], v[178:181], v[144:147], v[26:29]
	v_mfma_f32_16x16x32_f16 v[50:53], v[178:181], v[194:197], v[34:37]
	s_setprio 0
	s_barrier
	s_nop 0
	ds_read_b128 v[34:37], v130 offset:16384
	ds_read_b128 v[164:167], v130 offset:17408
	ds_read_b128 v[174:177], v108 offset:16384
	ds_read_b128 v[178:181], v108 offset:17408
	s_waitcnt vmcnt(12)
	s_barrier
	s_waitcnt lgkmcnt(0)
	s_setprio 1
	s_waitcnt lgkmcnt(0)
	v_mfma_f32_16x16x32_f16 v[22:25], v[34:37], v[138:141], v[22:25]
	v_mfma_f32_16x16x32_f16 v[198:201], v[164:167], v[148:151], v[22:25]
	v_mfma_f32_16x16x32_f16 v[22:25], v[34:37], v[152:155], v[30:33]
	v_mfma_f32_16x16x32_f16 v[30:33], v[164:167], v[156:159], v[22:25]
	v_mfma_f32_16x16x32_f16 v[22:25], v[174:177], v[110:113], v[38:41]
	v_mfma_f32_16x16x32_f16 v[14:17], v[34:37], v[110:113], v[14:17]
	v_mfma_f32_16x16x32_f16 v[110:113], v[178:181], v[114:117], v[22:25]
	v_mfma_f32_16x16x32_f16 v[22:25], v[174:177], v[138:141], v[54:57]
	v_mfma_f32_16x16x32_f16 v[14:17], v[164:167], v[114:117], v[14:17]
	v_mfma_f32_16x16x32_f16 v[54:57], v[178:181], v[148:151], v[22:25]
	v_mfma_f32_16x16x32_f16 v[22:25], v[174:177], v[152:155], v[62:65]
	v_mfma_f32_16x16x32_f16 v[114:117], v[178:181], v[156:159], v[22:25]
	s_setprio 0
	s_setprio 1
	v_mfma_f32_16x16x32_f16 v[22:25], v[34:37], v[46:49], v[42:45]
	v_mfma_f32_16x16x32_f16 v[138:141], v[164:167], v[144:147], v[22:25]
	v_mfma_f32_16x16x32_f16 v[22:25], v[34:37], v[182:185], v[58:61]
	v_mfma_f32_16x16x32_f16 v[148:151], v[164:167], v[186:189], v[22:25]
	v_mfma_f32_16x16x32_f16 v[22:25], v[34:37], v[190:193], v[66:69]
	v_mfma_f32_16x16x32_f16 v[152:155], v[164:167], v[194:197], v[22:25]
	v_mfma_f32_16x16x32_f16 v[22:25], v[174:177], v[46:49], v[70:73]
	v_mfma_f32_16x16x32_f16 v[142:145], v[178:181], v[144:147], v[22:25]
	v_mfma_f32_16x16x32_f16 v[22:25], v[174:177], v[182:185], v[78:81]
	v_mfma_f32_16x16x32_f16 v[156:159], v[178:181], v[186:189], v[22:25]
	v_mfma_f32_16x16x32_f16 v[22:25], v[174:177], v[190:193], v[82:85]
	v_mfma_f32_16x16x32_f16 v[164:167], v[178:181], v[194:197], v[22:25]
	s_setprio 0
	s_barrier
	ds_read_b128 v[58:61], v136
	ds_read_b128 v[174:177], v136 offset:1024
	ds_read_b128 v[178:181], v136 offset:2048
	ds_read_b128 v[182:185], v136 offset:3072
	ds_read_b128 v[186:189], v136 offset:4096
	ds_read_b128 v[134:137], v136 offset:5120
	ds_read_b128 v[34:37], v130 offset:32768
	ds_read_b128 v[62:65], v130 offset:33792
	ds_read_b128 v[78:81], v108 offset:32768
	ds_read_b128 v[190:193], v108 offset:33792
	s_waitcnt vmcnt(2)
	s_barrier
	s_waitcnt lgkmcnt(0)
	s_setprio 1
	s_waitcnt lgkmcnt(0)
	v_mfma_f32_16x16x32_f16 v[22:25], v[34:37], v[58:61], v[94:97]
	v_mfma_f32_16x16x32_f16 v[82:85], v[62:65], v[174:177], v[22:25]
	v_mfma_f32_16x16x32_f16 v[22:25], v[34:37], v[178:181], v[90:93]
	v_mfma_f32_16x16x32_f16 v[70:73], v[62:65], v[182:185], v[22:25]
	v_mfma_f32_16x16x32_f16 v[22:25], v[34:37], v[186:189], v[86:89]
	v_mfma_f32_16x16x32_f16 v[46:49], v[62:65], v[134:137], v[22:25]
	v_mfma_f32_16x16x32_f16 v[22:25], v[78:81], v[58:61], v[74:77]
	v_mfma_f32_16x16x32_f16 v[86:89], v[190:193], v[174:177], v[22:25]
	v_mfma_f32_16x16x32_f16 v[22:25], v[78:81], v[178:181], v[100:103]
	v_mfma_f32_16x16x32_f16 v[18:21], v[78:81], v[186:189], v[18:21]
	v_mfma_f32_16x16x32_f16 v[66:69], v[190:193], v[182:185], v[22:25]
	v_mfma_f32_16x16x32_f16 v[42:45], v[190:193], v[134:137], v[18:21]
	s_setprio 0
	s_barrier
	ds_read_b128 v[100:103], v133
	ds_read_b128 v[194:197], v133 offset:1024
	ds_read_b128 v[202:205], v133 offset:2048
	ds_read_b128 v[206:209], v133 offset:3072
	ds_read_b128 v[210:213], v133 offset:4096
	ds_read_b128 v[214:217], v133 offset:5120
	s_waitcnt vmcnt(0)
	s_barrier
	s_waitcnt lgkmcnt(0)
	s_setprio 1
	s_waitcnt lgkmcnt(0)
	v_mfma_f32_16x16x32_f16 v[6:9], v[34:37], v[202:205], v[6:9]
	v_mfma_f32_16x16x32_f16 v[2:5], v[34:37], v[210:213], v[2:5]
	v_mfma_f32_16x16x32_f16 v[22:25], v[62:65], v[206:209], v[6:9]
	v_mfma_f32_16x16x32_f16 v[6:9], v[62:65], v[214:217], v[2:5]
	v_mfma_f32_16x16x32_f16 v[2:5], v[78:81], v[100:103], v[26:29]
	v_mfma_f32_16x16x32_f16 v[10:13], v[34:37], v[100:103], v[10:13]
	v_mfma_f32_16x16x32_f16 v[34:37], v[190:193], v[194:197], v[2:5]
	v_mfma_f32_16x16x32_f16 v[2:5], v[78:81], v[202:205], v[160:163]
	v_mfma_f32_16x16x32_f16 v[18:21], v[190:193], v[206:209], v[2:5]
	v_mfma_f32_16x16x32_f16 v[2:5], v[78:81], v[210:213], v[50:53]
	v_mfma_f32_16x16x32_f16 v[38:41], v[62:65], v[194:197], v[10:13]
	v_mfma_f32_16x16x32_f16 v[2:5], v[190:193], v[214:217], v[2:5]
	s_setprio 0
	s_barrier
	ds_read_b128 v[10:13], v130 offset:49152
	ds_read_b128 v[26:29], v130 offset:50176
	ds_read_b128 v[128:131], v108 offset:49152
	ds_read_b128 v[160:163], v108 offset:50176
	s_barrier
	s_waitcnt lgkmcnt(0)
	s_setprio 1
	s_waitcnt lgkmcnt(0)
	v_mfma_f32_16x16x32_f16 v[14:17], v[10:13], v[58:61], v[14:17]
	v_mfma_f32_16x16x32_f16 v[90:93], v[26:29], v[174:177], v[14:17]
	v_mfma_f32_16x16x32_f16 v[14:17], v[10:13], v[178:181], v[198:201]
	v_mfma_f32_16x16x32_f16 v[78:81], v[26:29], v[182:185], v[14:17]
	v_mfma_f32_16x16x32_f16 v[14:17], v[10:13], v[186:189], v[30:33]
	v_mfma_f32_16x16x32_f16 v[62:65], v[26:29], v[134:137], v[14:17]
	v_mfma_f32_16x16x32_f16 v[14:17], v[128:131], v[58:61], v[110:113]
	v_mfma_f32_16x16x32_f16 v[94:97], v[160:163], v[174:177], v[14:17]
	v_mfma_f32_16x16x32_f16 v[14:17], v[128:131], v[178:181], v[54:57]
	v_mfma_f32_16x16x32_f16 v[74:77], v[160:163], v[182:185], v[14:17]
	v_mfma_f32_16x16x32_f16 v[14:17], v[128:131], v[186:189], v[114:117]
	v_mfma_f32_16x16x32_f16 v[58:61], v[160:163], v[134:137], v[14:17]
	s_setprio 0
	s_setprio 1
	v_mfma_f32_16x16x32_f16 v[14:17], v[10:13], v[100:103], v[138:141]
	v_mfma_f32_16x16x32_f16 v[54:57], v[26:29], v[194:197], v[14:17]
	v_mfma_f32_16x16x32_f16 v[14:17], v[10:13], v[202:205], v[148:151]
	v_mfma_f32_16x16x32_f16 v[10:13], v[10:13], v[210:213], v[152:155]
	v_mfma_f32_16x16x32_f16 v[30:33], v[26:29], v[206:209], v[14:17]
	v_mfma_f32_16x16x32_f16 v[14:17], v[26:29], v[214:217], v[10:13]
	v_mfma_f32_16x16x32_f16 v[10:13], v[128:131], v[100:103], v[142:145]
	v_mfma_f32_16x16x32_f16 v[50:53], v[160:163], v[194:197], v[10:13]
	v_mfma_f32_16x16x32_f16 v[10:13], v[128:131], v[202:205], v[156:159]
	v_mfma_f32_16x16x32_f16 v[26:29], v[160:163], v[206:209], v[10:13]
	v_mfma_f32_16x16x32_f16 v[10:13], v[128:131], v[210:213], v[164:167]
	v_mfma_f32_16x16x32_f16 v[10:13], v[160:163], v[214:217], v[10:13]
	s_setprio 0
	s_movk_i32 s0, 0x100
	v_cmp_gt_u32_e64 s[0:1], s0, v107
	s_barrier
	s_and_saveexec_b64 s[2:3], s[0:1]
	s_cbranch_execz .LBB1_69
	s_barrier
